# speedup vs baseline: 1.0069x; 1.0069x over previous
_Z10giou_finalPK15HIP_vector_typeIfLj2EEPf:
	s_load_dwordx4 s[12:15], s[0:1], 0x0
	v_lshlrev_b32_e32 v1, 4, v0
	v_cmp_eq_u32_e32 vcc, 0, v0
	s_waitcnt lgkmcnt(0)
	global_load_dwordx4 v[2:5], v1, s[12:13]
	global_load_dwordx4 v[6:9], v1, s[12:13] offset:1024
	s_waitcnt vmcnt(1)
	v_add_f32_e32 v1, v2, v4
	v_add_f32_e32 v2, v3, v5
	s_waitcnt vmcnt(0)
	v_add_f32_e32 v3, v6, v8
	v_add_f32_e32 v4, v7, v9
	v_add_f32_e32 v1, v1, v3
	v_add_f32_e32 v2, v2, v4
	s_nop 0
	v_add_f32_dpp v1, v1, v1 quad_perm:[1,0,3,2] row_mask:0xf bank_mask:0xf bound_ctrl:1
	v_add_f32_dpp v2, v2, v2 quad_perm:[1,0,3,2] row_mask:0xf bank_mask:0xf bound_ctrl:1
	s_nop 0
	v_add_f32_dpp v1, v1, v1 quad_perm:[2,3,0,1] row_mask:0xf bank_mask:0xf bound_ctrl:1
	v_add_f32_dpp v2, v2, v2 quad_perm:[2,3,0,1] row_mask:0xf bank_mask:0xf bound_ctrl:1
	s_nop 0
	v_add_f32_dpp v1, v1, v1 row_half_mirror row_mask:0xf bank_mask:0xf bound_ctrl:1
	v_add_f32_dpp v2, v2, v2 row_half_mirror row_mask:0xf bank_mask:0xf bound_ctrl:1
	s_nop 0
	v_add_f32_dpp v1, v1, v1 row_mirror row_mask:0xf bank_mask:0xf bound_ctrl:1
	v_add_f32_dpp v2, v2, v2 row_mirror row_mask:0xf bank_mask:0xf bound_ctrl:1
	v_readlane_b32 s2, v1, 0
	v_readlane_b32 s5, v1, 16
	v_readlane_b32 s3, v1, 32
	v_readlane_b32 s4, v1, 48
	v_readlane_b32 s6, v2, 0
	v_readlane_b32 s9, v2, 16
	v_readlane_b32 s7, v2, 32
	v_readlane_b32 s8, v2, 48
	s_and_saveexec_b64 s[10:11], vcc
	s_cbranch_execz .LBB1_2
	v_mov_b32_e32 v0, s9
	v_add_f32_e32 v0, s6, v0
	v_mov_b32_e32 v1, s5
	v_add_f32_e32 v0, s7, v0
	v_add_f32_e32 v1, s2, v1
	v_add_f32_e32 v0, s8, v0
	v_add_f32_e32 v1, s3, v1
	v_add_f32_e32 v1, s4, v1
	v_max_f32_e32 v0, 1.0, v0
	v_div_scale_f32 v2, s[2:3], v0, v0, v1
	v_rcp_f32_e32 v3, v2
	s_nop 0
	v_fma_f32 v4, -v2, v3, 1.0
	v_fmac_f32_e32 v3, v4, v3
	v_div_scale_f32 v4, vcc, v1, v0, v1
	v_mul_f32_e32 v5, v4, v3
	v_fma_f32 v6, -v2, v5, v4
	v_fmac_f32_e32 v5, v6, v3
	v_fma_f32 v2, -v2, v5, v4
	v_div_fmas_f32 v2, v2, v3, v5
	v_div_fixup_f32 v0, v2, v0, v1
	v_mov_b32_e32 v1, 0
	global_store_dword v1, v0, s[14:15]

	.amdhsa_kernel _Z10giou_finalPK15HIP_vector_typeIfLj2EEPf
		.amdhsa_group_segment_fixed_size 0
		.amdhsa_private_segment_fixed_size 0
		.amdhsa_kernarg_size 16
		.amdhsa_user_sgpr_count 2
		.amdhsa_user_sgpr_dispatch_ptr 0
		.amdhsa_user_sgpr_queue_ptr 0
		.amdhsa_user_sgpr_kernarg_segment_ptr 1
		.amdhsa_user_sgpr_dispatch_id 0
		.amdhsa_user_sgpr_kernarg_preload_length 0
		.amdhsa_user_sgpr_kernarg_preload_offset 0
		.amdhsa_user_sgpr_private_segment_size 0
		.amdhsa_uses_dynamic_stack 0
		.amdhsa_enable_private_segment 0
		.amdhsa_system_sgpr_workgroup_id_x 1
		.amdhsa_system_sgpr_workgroup_id_y 0
		.amdhsa_system_sgpr_workgroup_id_z 0
		.amdhsa_system_sgpr_workgroup_info 0
		.amdhsa_system_vgpr_workitem_id 0
		.amdhsa_next_free_vgpr 18
		.amdhsa_next_free_sgpr 16
		.amdhsa_accum_offset 20
		.amdhsa_reserve_vcc 1
		.amdhsa_float_round_mode_32 0
		.amdhsa_float_round_mode_16_64 0
		.amdhsa_float_denorm_mode_32 3
		.amdhsa_float_denorm_mode_16_64 3
		.amdhsa_dx10_clamp 1
		.amdhsa_ieee_mode 1
		.amdhsa_fp16_overflow 0
		.amdhsa_tg_split 0
		.amdhsa_exception_fp_ieee_invalid_op 0
		.amdhsa_exception_fp_denorm_src 0
		.amdhsa_exception_fp_ieee_div_zero 0
		.amdhsa_exception_fp_ieee_overflow 0
		.amdhsa_exception_fp_ieee_underflow 0
		.amdhsa_exception_fp_ieee_inexact 0
		.amdhsa_exception_int_div_zero 0
	.end_amdhsa_kernel

.Lfunc_end1:
	.size	_Z10giou_finalPK15HIP_vector_typeIfLj2EEPf, .Lfunc_end1-_Z10giou_finalPK15HIP_vector_typeIfLj2EEPf
	.set _Z10giou_finalPK15HIP_vector_typeIfLj2EEPf.num_vgpr, 18
	.set _Z10giou_finalPK15HIP_vector_typeIfLj2EEPf.num_agpr, 0
	.set _Z10giou_finalPK15HIP_vector_typeIfLj2EEPf.numbered_sgpr, 16
	.set _Z10giou_finalPK15HIP_vector_typeIfLj2EEPf.num_named_barrier, 0
	.set _Z10giou_finalPK15HIP_vector_typeIfLj2EEPf.private_seg_size, 0
	.set _Z10giou_finalPK15HIP_vector_typeIfLj2EEPf.uses_vcc, 1
	.set _Z10giou_finalPK15HIP_vector_typeIfLj2EEPf.uses_flat_scratch, 0
	.set _Z10giou_finalPK15HIP_vector_typeIfLj2EEPf.has_dyn_sized_stack, 0
	.set _Z10giou_finalPK15HIP_vector_typeIfLj2EEPf.has_recursion, 0
	.set _Z10giou_finalPK15HIP_vector_typeIfLj2EEPf.has_indirect_call, 0

amdhsa.kernels:
  - .agpr_count:     0
    .args:
      - .actual_access:  read_only
        .address_space:  global
        .offset:         0
        .size:           8
        .value_kind:     global_buffer
      - .actual_access:  read_only
        .address_space:  global
        .offset:         8
        .size:           8
        .value_kind:     global_buffer
      - .actual_access:  read_only
        .address_space:  global
        .offset:         16
        .size:           8
        .value_kind:     global_buffer
      - .actual_access:  read_only
        .address_space:  global
        .offset:         24
        .size:           8
        .value_kind:     global_buffer
      - .actual_access:  write_only
        .address_space:  global
        .offset:         32
        .size:           8
        .value_kind:     global_buffer
    .group_segment_fixed_size: 49280
    .kernarg_segment_align: 8
    .kernarg_segment_size: 40
    .language:       OpenCL C
    .language_version:
      - 2
      - 0
    .max_flat_workgroup_size: 1024
    .name:           _Z12giou_partialPK15HIP_vector_typeIfLj4EES2_S2_PKiPS_IfLj2EE
    .private_segment_fixed_size: 0
    .sgpr_count:     40
    .sgpr_spill_count: 0
    .symbol:         _Z12giou_partialPK15HIP_vector_typeIfLj4EES2_S2_PKiPS_IfLj2EE.kd
    .uniform_work_group_size: 1
    .uses_dynamic_stack: false
    .vgpr_count:     60
    .vgpr_spill_count: 0
    .wavefront_size: 64
  - .agpr_count:     0
    .args:
      - .actual_access:  read_only
        .address_space:  global
        .offset:         0
        .size:           8
        .value_kind:     global_buffer
      - .actual_access:  write_only
        .address_space:  global
        .offset:         8
        .size:           8
        .value_kind:     global_buffer
    .group_segment_fixed_size: 0
    .kernarg_segment_align: 8
    .kernarg_segment_size: 16
    .language:       OpenCL C
    .language_version:
      - 2
      - 0
    .max_flat_workgroup_size: 64
    .name:           _Z10giou_finalPK15HIP_vector_typeIfLj2EEPf
    .private_segment_fixed_size: 0
    .sgpr_count:     22
    .sgpr_spill_count: 0
    .symbol:         _Z10giou_finalPK15HIP_vector_typeIfLj2EEPf.kd
    .uniform_work_group_size: 1
    .uses_dynamic_stack: false
    .vgpr_count:     18
    .vgpr_spill_count: 0
    .wavefront_size: 64
